# attention unit edges: output-store acknowledgement no longer waited before the unit barrier / next unit's Q loads
# speedup vs baseline: 1.0092x; 1.0021x over previous
.LBB0_1164:
	s_or_b64 exec, exec, s[6:7]
	s_waitcnt lgkmcnt(0)
	v_add_u32_e32 v74, s69, v134
	ds_read_b128 v[66:69], v74
	ds_read_b128 v[70:73], v74 offset:32
	s_mulk_i32 s51, 0x2200
	s_add_i32 s4, s51, 0
	v_mul_u32_u24_e32 v83, 0x440, v153
	s_waitcnt lgkmcnt(0)
	v_rcp_f32_e32 v75, v66
	v_rcp_f32_e32 v76, v67
	v_rcp_f32_e32 v77, v68
	v_rcp_f32_e32 v78, v69
	v_rcp_f32_e32 v79, v70
	ds_read_b128 v[66:69], v74 offset:64
	v_rcp_f32_e32 v80, v71
	v_rcp_f32_e32 v81, v72
	v_rcp_f32_e32 v82, v73
	ds_read_b128 v[70:73], v74 offset:96
	v_lshlrev_b32_e32 v74, 1, v152
	v_mul_f32_e32 v2, v2, v75
	v_add3_u32 v74, s4, v74, v83
	v_bfe_u32 v83, v2, 16, 1
	v_add3_u32 v2, v2, v83, s58
	ds_write_b16_d16_hi v74, v2 offset:32768
	v_mul_f32_e32 v2, v50, v75
	v_bfe_u32 v50, v2, 16, 1
	v_add3_u32 v2, v2, v50, s58
	ds_write_b16_d16_hi v74, v2 offset:32832
	v_mul_f32_e32 v2, v34, v75
	v_bfe_u32 v34, v2, 16, 1
	v_add3_u32 v2, v2, v34, s58
	ds_write_b16_d16_hi v74, v2 offset:32896
	v_mul_f32_e32 v2, v18, v75
	v_bfe_u32 v18, v2, 16, 1
	v_add3_u32 v2, v2, v18, s58
	ds_write_b16_d16_hi v74, v2 offset:32960
	v_mul_f32_e32 v2, v3, v76
	v_bfe_u32 v3, v2, 16, 1
	v_add3_u32 v2, v2, v3, s58
	ds_write_b16_d16_hi v74, v2 offset:33040
	v_mul_f32_e32 v2, v51, v76
	v_bfe_u32 v3, v2, 16, 1
	v_add3_u32 v2, v2, v3, s58
	ds_write_b16_d16_hi v74, v2 offset:33104
	v_mul_f32_e32 v2, v35, v76
	v_bfe_u32 v3, v2, 16, 1
	v_add3_u32 v2, v2, v3, s58
	ds_write_b16_d16_hi v74, v2 offset:33168
	v_mul_f32_e32 v2, v19, v76
	v_bfe_u32 v3, v2, 16, 1
	v_add3_u32 v2, v2, v3, s58
	ds_write_b16_d16_hi v74, v2 offset:33232
	v_mul_f32_e32 v2, v4, v77
	v_bfe_u32 v3, v2, 16, 1
	v_add3_u32 v2, v2, v3, s58
	ds_write_b16_d16_hi v74, v2 offset:33312
	v_mul_f32_e32 v2, v52, v77
	v_bfe_u32 v3, v2, 16, 1
	v_add3_u32 v2, v2, v3, s58
	ds_write_b16_d16_hi v74, v2 offset:33376
	v_mul_f32_e32 v2, v36, v77
	v_bfe_u32 v3, v2, 16, 1
	v_add3_u32 v2, v2, v3, s58
	ds_write_b16_d16_hi v74, v2 offset:33440
	v_mul_f32_e32 v2, v20, v77
	v_bfe_u32 v3, v2, 16, 1
	v_add3_u32 v2, v2, v3, s58
	ds_write_b16_d16_hi v74, v2 offset:33504
	v_mul_f32_e32 v2, v5, v78
	v_bfe_u32 v3, v2, 16, 1
	v_add3_u32 v2, v2, v3, s58
	ds_write_b16_d16_hi v74, v2 offset:33584
	v_mul_f32_e32 v2, v53, v78
	v_bfe_u32 v3, v2, 16, 1
	v_add3_u32 v2, v2, v3, s58
	ds_write_b16_d16_hi v74, v2 offset:33648
	v_mul_f32_e32 v2, v37, v78
	v_bfe_u32 v3, v2, 16, 1
	v_add3_u32 v2, v2, v3, s58
	ds_write_b16_d16_hi v74, v2 offset:33712
	v_mul_f32_e32 v2, v21, v78
	v_bfe_u32 v3, v2, 16, 1
	v_add3_u32 v2, v2, v3, s58
	ds_write_b16_d16_hi v74, v2 offset:33776
	v_mul_f32_e32 v2, v6, v79
	v_bfe_u32 v3, v2, 16, 1
	v_add3_u32 v2, v2, v3, s58
	ds_write_b16_d16_hi v74, v2 offset:34944
	v_mul_f32_e32 v2, v54, v79
	v_bfe_u32 v3, v2, 16, 1
	v_add3_u32 v2, v2, v3, s58
	ds_write_b16_d16_hi v74, v2 offset:35008
	v_mul_f32_e32 v2, v38, v79
	v_bfe_u32 v3, v2, 16, 1
	v_add3_u32 v2, v2, v3, s58
	ds_write_b16_d16_hi v74, v2 offset:35072
	v_mul_f32_e32 v2, v22, v79
	v_bfe_u32 v3, v2, 16, 1
	v_add3_u32 v2, v2, v3, s58
	ds_write_b16_d16_hi v74, v2 offset:35136
	v_mul_f32_e32 v2, v7, v80
	v_bfe_u32 v3, v2, 16, 1
	v_add3_u32 v2, v2, v3, s58
	ds_write_b16_d16_hi v74, v2 offset:35216
	v_mul_f32_e32 v2, v55, v80
	v_bfe_u32 v3, v2, 16, 1
	v_add3_u32 v2, v2, v3, s58
	ds_write_b16_d16_hi v74, v2 offset:35280
	v_mul_f32_e32 v2, v39, v80
	v_bfe_u32 v3, v2, 16, 1
	v_add3_u32 v2, v2, v3, s58
	ds_write_b16_d16_hi v74, v2 offset:35344
	v_mul_f32_e32 v2, v23, v80
	v_bfe_u32 v3, v2, 16, 1
	v_add3_u32 v2, v2, v3, s58
	ds_write_b16_d16_hi v74, v2 offset:35408
	v_mul_f32_e32 v2, v8, v81
	v_bfe_u32 v3, v2, 16, 1
	v_add3_u32 v2, v2, v3, s58
	ds_write_b16_d16_hi v74, v2 offset:35488
	v_mul_f32_e32 v2, v56, v81
	v_bfe_u32 v3, v2, 16, 1
	v_add3_u32 v2, v2, v3, s58
	ds_write_b16_d16_hi v74, v2 offset:35552
	v_mul_f32_e32 v2, v40, v81
	v_bfe_u32 v3, v2, 16, 1
	v_add3_u32 v2, v2, v3, s58
	ds_write_b16_d16_hi v74, v2 offset:35616
	v_mul_f32_e32 v2, v24, v81
	v_bfe_u32 v3, v2, 16, 1
	v_add3_u32 v2, v2, v3, s58
	ds_write_b16_d16_hi v74, v2 offset:35680
	v_mul_f32_e32 v2, v9, v82
	v_bfe_u32 v3, v2, 16, 1
	v_add3_u32 v2, v2, v3, s58
	ds_write_b16_d16_hi v74, v2 offset:35760
	v_mul_f32_e32 v2, v57, v82
	v_bfe_u32 v3, v2, 16, 1
	v_add3_u32 v2, v2, v3, s58
	ds_write_b16_d16_hi v74, v2 offset:35824
	v_mul_f32_e32 v2, v41, v82
	v_bfe_u32 v3, v2, 16, 1
	s_waitcnt lgkmcnt(0)
	v_rcp_f32_e32 v66, v66
	v_add3_u32 v2, v2, v3, s58
	ds_write_b16_d16_hi v74, v2 offset:35888
	v_mul_f32_e32 v2, v25, v82
	v_bfe_u32 v3, v2, 16, 1
	v_add3_u32 v2, v2, v3, s58
	ds_write_b16_d16_hi v74, v2 offset:35952
	v_mul_f32_e32 v2, v10, v66
	v_bfe_u32 v3, v2, 16, 1
	v_add3_u32 v2, v2, v3, s58
	ds_write_b16_d16_hi v74, v2 offset:37120
	v_mul_f32_e32 v2, v58, v66
	v_bfe_u32 v3, v2, 16, 1
	v_add3_u32 v2, v2, v3, s58
	ds_write_b16_d16_hi v74, v2 offset:37184
	v_mul_f32_e32 v2, v42, v66
	v_bfe_u32 v3, v2, 16, 1
	v_rcp_f32_e32 v67, v67
	v_add3_u32 v2, v2, v3, s58
	ds_write_b16_d16_hi v74, v2 offset:37248
	v_mul_f32_e32 v2, v26, v66
	v_bfe_u32 v3, v2, 16, 1
	v_add3_u32 v2, v2, v3, s58
	ds_write_b16_d16_hi v74, v2 offset:37312
	v_mul_f32_e32 v2, v11, v67
	v_bfe_u32 v3, v2, 16, 1
	v_add3_u32 v2, v2, v3, s58
	ds_write_b16_d16_hi v74, v2 offset:37392
	v_mul_f32_e32 v2, v59, v67
	v_bfe_u32 v3, v2, 16, 1
	v_add3_u32 v2, v2, v3, s58
	ds_write_b16_d16_hi v74, v2 offset:37456
	v_mul_f32_e32 v2, v43, v67
	v_bfe_u32 v3, v2, 16, 1
	v_rcp_f32_e32 v68, v68
	v_add3_u32 v2, v2, v3, s58
	ds_write_b16_d16_hi v74, v2 offset:37520
	v_mul_f32_e32 v2, v27, v67
	v_bfe_u32 v3, v2, 16, 1
	v_add3_u32 v2, v2, v3, s58
	ds_write_b16_d16_hi v74, v2 offset:37584
	v_mul_f32_e32 v2, v12, v68
	v_bfe_u32 v3, v2, 16, 1
	v_add3_u32 v2, v2, v3, s58
	ds_write_b16_d16_hi v74, v2 offset:37664
	v_mul_f32_e32 v2, v60, v68
	v_bfe_u32 v3, v2, 16, 1
	v_add3_u32 v2, v2, v3, s58
	ds_write_b16_d16_hi v74, v2 offset:37728
	v_mul_f32_e32 v2, v44, v68
	v_bfe_u32 v3, v2, 16, 1
	v_rcp_f32_e32 v69, v69
	v_add3_u32 v2, v2, v3, s58
	ds_write_b16_d16_hi v74, v2 offset:37792
	v_mul_f32_e32 v2, v28, v68
	v_bfe_u32 v3, v2, 16, 1
	v_add3_u32 v2, v2, v3, s58
	ds_write_b16_d16_hi v74, v2 offset:37856
	v_mul_f32_e32 v2, v13, v69
	v_bfe_u32 v3, v2, 16, 1
	v_add3_u32 v2, v2, v3, s58
	ds_write_b16_d16_hi v74, v2 offset:37936
	v_mul_f32_e32 v2, v61, v69
	v_bfe_u32 v3, v2, 16, 1
	v_add3_u32 v2, v2, v3, s58
	ds_write_b16_d16_hi v74, v2 offset:38000
	v_mul_f32_e32 v2, v45, v69
	v_bfe_u32 v3, v2, 16, 1
	v_rcp_f32_e32 v70, v70
	v_add3_u32 v2, v2, v3, s58
	ds_write_b16_d16_hi v74, v2 offset:38064
	v_mul_f32_e32 v2, v29, v69
	v_bfe_u32 v3, v2, 16, 1
	v_add3_u32 v2, v2, v3, s58
	ds_write_b16_d16_hi v74, v2 offset:38128
	v_mul_f32_e32 v2, v14, v70
	v_bfe_u32 v3, v2, 16, 1
	v_add3_u32 v2, v2, v3, s58
	ds_write_b16_d16_hi v74, v2 offset:39296
	v_mul_f32_e32 v2, v62, v70
	v_bfe_u32 v3, v2, 16, 1
	v_add3_u32 v2, v2, v3, s58
	ds_write_b16_d16_hi v74, v2 offset:39360
	v_mul_f32_e32 v2, v46, v70
	v_bfe_u32 v3, v2, 16, 1
	v_rcp_f32_e32 v71, v71
	v_add3_u32 v2, v2, v3, s58
	ds_write_b16_d16_hi v74, v2 offset:39424
	v_mul_f32_e32 v2, v30, v70
	v_bfe_u32 v3, v2, 16, 1
	v_add3_u32 v2, v2, v3, s58
	ds_write_b16_d16_hi v74, v2 offset:39488
	v_mul_f32_e32 v2, v15, v71
	v_bfe_u32 v3, v2, 16, 1
	v_add3_u32 v2, v2, v3, s58
	ds_write_b16_d16_hi v74, v2 offset:39568
	v_mul_f32_e32 v2, v63, v71
	v_bfe_u32 v3, v2, 16, 1
	v_add3_u32 v2, v2, v3, s58
	ds_write_b16_d16_hi v74, v2 offset:39632
	v_mul_f32_e32 v2, v47, v71
	v_bfe_u32 v3, v2, 16, 1
	v_rcp_f32_e32 v72, v72
	v_add3_u32 v2, v2, v3, s58
	ds_write_b16_d16_hi v74, v2 offset:39696
	v_mul_f32_e32 v2, v31, v71
	v_bfe_u32 v3, v2, 16, 1
	v_add3_u32 v2, v2, v3, s58
	ds_write_b16_d16_hi v74, v2 offset:39760
	v_mul_f32_e32 v2, v16, v72
	v_bfe_u32 v3, v2, 16, 1
	v_add3_u32 v2, v2, v3, s58
	ds_write_b16_d16_hi v74, v2 offset:39840
	v_mul_f32_e32 v2, v64, v72
	v_bfe_u32 v3, v2, 16, 1
	v_add3_u32 v2, v2, v3, s58
	ds_write_b16_d16_hi v74, v2 offset:39904
	v_mul_f32_e32 v2, v48, v72
	v_bfe_u32 v3, v2, 16, 1
	v_rcp_f32_e32 v73, v73
	v_add3_u32 v2, v2, v3, s58
	ds_write_b16_d16_hi v74, v2 offset:39968
	v_mul_f32_e32 v2, v32, v72
	v_bfe_u32 v3, v2, 16, 1
	v_add3_u32 v2, v2, v3, s58
	ds_write_b16_d16_hi v74, v2 offset:40032
	v_mul_f32_e32 v2, v17, v73
	v_bfe_u32 v3, v2, 16, 1
	v_add3_u32 v2, v2, v3, s58
	ds_write_b16_d16_hi v74, v2 offset:40112
	v_mul_f32_e32 v2, v65, v73
	v_bfe_u32 v3, v2, 16, 1
	v_add3_u32 v2, v2, v3, s58
	ds_write_b16_d16_hi v74, v2 offset:40176
	v_mul_f32_e32 v2, v49, v73
	v_bfe_u32 v3, v2, 16, 1
	v_add3_u32 v2, v2, v3, s58
	ds_write_b16_d16_hi v74, v2 offset:40240
	v_mul_f32_e32 v2, v33, v73
	v_bfe_u32 v3, v2, 16, 1
	v_add3_u32 v2, v2, v3, s58
	s_ashr_i32 s51, s50, 31
	ds_write_b16_d16_hi v74, v2 offset:40304
	s_lshl_b64 s[6:7], s[50:51], 11
	v_lshlrev_b32_e32 v2, 4, v151
	v_lshrrev_b32_e32 v6, 4, v154
	s_add_u32 s5, s49, s6
	v_and_b32_e32 v134, 0xf0, v2
	v_mul_u32_u24_e32 v2, 0x110, v6
	s_waitcnt lgkmcnt(0)
	s_addc_u32 s7, s52, s7
	v_add3_u32 v14, s4, v134, v2
	s_add_u32 s6, s5, s46
	ds_read_b128 v[2:5], v14 offset:32768
	s_addc_u32 s7, s7, 0
	v_lshl_add_u64 v[10:11], s[6:7], 0, v[134:135]
	v_lshlrev_b32_e32 v134, 11, v6
	ds_read_b128 v[6:9], v14 offset:33856
	v_lshl_add_u64 v[12:13], v[10:11], 0, v[134:135]
	s_waitcnt lgkmcnt(0)
	global_store_dwordx4 v[12:13], v[2:5], off
	s_add_i32 s67, s67, 1
	s_mul_i32 s4, s67, s34
	v_or_b32_e32 v2, 0x2000, v134
	v_mov_b32_e32 v3, v135
	v_lshl_add_u64 v[2:3], v[10:11], 0, v[2:3]
	global_store_dwordx4 v[2:3], v[6:9], off
	ds_read_b128 v[2:5], v14 offset:34944
	s_add_i32 s7, s4, s89
	v_or_b32_e32 v6, 0x4000, v134
	v_mov_b32_e32 v7, v135
	v_lshl_add_u64 v[12:13], v[10:11], 0, v[6:7]
	ds_read_b128 v[6:9], v14 offset:36032
	s_waitcnt lgkmcnt(0)
	global_store_dwordx4 v[12:13], v[2:5], off
	s_cmpk_lt_i32 s7, 0x220
	s_nop 0
	v_or_b32_e32 v2, 0x6000, v134
	v_mov_b32_e32 v3, v135
	v_lshl_add_u64 v[2:3], v[10:11], 0, v[2:3]
	global_store_dwordx4 v[2:3], v[6:9], off
	ds_read_b128 v[2:5], v14 offset:37120
	s_nop 0
	v_or_b32_e32 v6, 0x8000, v134
	v_mov_b32_e32 v7, v135
	v_lshl_add_u64 v[12:13], v[10:11], 0, v[6:7]
	ds_read_b128 v[6:9], v14 offset:38208
	s_waitcnt lgkmcnt(0)
	global_store_dwordx4 v[12:13], v[2:5], off
	v_or_b32_e32 v12, 0xc000, v134
	v_mov_b32_e32 v13, v135
	v_or_b32_e32 v2, 0xa000, v134
	v_mov_b32_e32 v3, v135
	v_lshl_add_u64 v[2:3], v[10:11], 0, v[2:3]
	global_store_dwordx4 v[2:3], v[6:9], off
	ds_read_b128 v[2:5], v14 offset:39296
	ds_read_b128 v[6:9], v14 offset:40384
	v_lshl_add_u64 v[12:13], v[10:11], 0, v[12:13]
	v_or_b32_e32 v134, 0xe000, v134
	s_waitcnt lgkmcnt(0)
	global_store_dwordx4 v[12:13], v[2:5], off
	s_nop 1
	v_lshl_add_u64 v[2:3], v[10:11], 0, v[134:135]
	global_store_dwordx4 v[2:3], v[6:9], off
	s_barrier
	s_cbranch_scc0 .LBB0_1189

.LBB0_1170:
	v_mov_b32_e32 v151, v0
	s_and_b32 s8, s7, 7
	s_mov_b64 s[10:11], s[42:43]
	v_readfirstlane_b32 s7, v151
	s_ashr_i32 s51, s7, 6
	s_lshl_b32 s5, s51, 5
	v_and_b32_e32 v152, 31, v151
	s_add_i32 s50, s5, s4
	v_add_u32_e32 v18, s50, v152
	v_mov_b64_e32 v[2:3], s[10:11]
	v_bfe_u32 v153, v151, 5, 1
	v_mad_i64_i32 v[2:3], s[4:5], v18, s53, v[2:3]
	s_mul_i32 s46, s8, 0x180
	v_lshl_add_u64 v[2:3], v[2:3], 0, s[46:47]
	v_lshlrev_b32_e32 v134, 4, v153
	v_lshl_add_u64 v[14:15], v[2:3], 0, v[134:135]
	flat_load_dwordx4 v[126:129], v[14:15]
	flat_load_dwordx4 v[122:125], v[14:15] offset:32
	flat_load_dwordx4 v[118:121], v[14:15] offset:64
	flat_load_dwordx4 v[114:117], v[14:15] offset:96
	flat_load_dwordx4 v[110:113], v[14:15] offset:128
	flat_load_dwordx4 v[106:109], v[14:15] offset:160
	flat_load_dwordx4 v[102:105], v[14:15] offset:192
	flat_load_dwordx4 v[98:101], v[14:15] offset:224
	flat_load_dwordx4 v[2:5], v[14:15] offset:256
	flat_load_dwordx4 v[6:9], v[14:15] offset:288
	flat_load_dwordx4 v[10:13], v[14:15] offset:320
	s_nop 0
	flat_load_dwordx4 v[14:17], v[14:15] offset:352
	v_cmp_lt_i32_e32 vcc, s55, v18
	s_and_saveexec_b64 s[4:5], vcc
	s_cbranch_execz .LBB0_1172
	v_add_u32_e32 v20, 0xc00, v18
	v_lshlrev_b32_e32 v19, 3, v153
	v_lshrrev_b32_e32 v20, 2, v20
	v_and_or_b32 v20, v20, s56, v19
	v_lshlrev_b32_e32 v32, 3, v20
	global_load_dwordx4 v[20:23], v32, s[44:45]
	global_load_dwordx4 v[24:27], v32, s[44:45] offset:16
	global_load_dwordx4 v[28:31], v32, s[44:45] offset:32
	s_nop 0
	global_load_dwordx4 v[32:35], v32, s[44:45] offset:48
	s_waitcnt vmcnt(0) lgkmcnt(0)
	v_and_b32_e32 v56, 0xffff0000, v4
	v_lshlrev_b32_e32 v57, 16, v4
	v_lshlrev_b32_e32 v4, 4, v18
	v_and_or_b32 v4, v4, s56, v19
	v_lshlrev_b32_e32 v4, 3, v4
	global_load_dwordx4 v[36:39], v4, s[44:45] offset:48
	global_load_dwordx4 v[40:43], v4, s[44:45] offset:32
	global_load_dwordx4 v[44:47], v4, s[44:45] offset:16
	global_load_dwordx4 v[48:51], v4, s[44:45]
	v_lshlrev_b32_e32 v53, 16, v3
	v_lshlrev_b32_e32 v52, 16, v2
	v_lshlrev_b32_e32 v55, 16, v7
	v_lshlrev_b32_e32 v54, 16, v6
	v_and_b32_e32 v3, 0xffff0000, v3
	v_and_b32_e32 v2, 0xffff0000, v2
	v_and_b32_e32 v7, 0xffff0000, v7
	v_and_b32_e32 v6, 0xffff0000, v6
	v_and_b32_e32 v58, 0xffff0000, v8
	v_lshlrev_b32_e32 v59, 16, v8
	v_and_b32_e32 v62, 0xffff0000, v9
	v_lshlrev_b32_e32 v63, 16, v9
	v_and_b32_e32 v60, 0xffff0000, v5
	v_lshlrev_b32_e32 v61, 16, v5
	v_mov_b32_e32 v8, v22
	v_mov_b32_e32 v9, v26
	v_mov_b32_e32 v26, v23
	v_mov_b32_e32 v19, v28
	v_mov_b32_e32 v28, v31
	v_mov_b32_e32 v5, v24
	v_mov_b32_e32 v24, v21
	v_mov_b32_e32 v18, v30
	v_pk_mul_f32 v[30:31], v[26:27], v[2:3]
	v_pk_mul_f32 v[26:27], v[26:27], v[6:7]
	v_pk_mul_f32 v[64:65], v[28:29], v[58:59]
	v_pk_mul_f32 v[28:29], v[28:29], v[56:57]
	v_mov_b32_e32 v4, v20
	v_pk_mul_f32 v[22:23], v[24:25], v[52:53]
	v_pk_mul_f32 v[24:25], v[24:25], v[54:55]
	v_pk_fma_f32 v[6:7], v[8:9], v[6:7], v[30:31]
	v_pk_fma_f32 v[2:3], v[8:9], v[2:3], v[26:27] neg_lo:[0,0,1] neg_hi:[0,0,1]
	v_pk_fma_f32 v[8:9], v[18:19], v[56:57], v[64:65] neg_lo:[0,0,1] neg_hi:[0,0,1]
	v_pk_fma_f32 v[18:19], v[18:19], v[58:59], v[28:29]
	v_mov_b32_e32 v21, v32
	v_pk_fma_f32 v[22:23], v[4:5], v[54:55], v[22:23]
	v_pk_fma_f32 v[4:5], v[4:5], v[52:53], v[24:25] neg_lo:[0,0,1] neg_hi:[0,0,1]
	v_and_b32_sdwa v31, v2, v1 dst_sel:DWORD dst_unused:UNUSED_PAD src0_sel:WORD_1 src1_sel:DWORD
	v_and_b32_sdwa v32, v9, v1 dst_sel:DWORD dst_unused:UNUSED_PAD src0_sel:WORD_1 src1_sel:DWORD
	v_and_b32_sdwa v52, v19, v1 dst_sel:DWORD dst_unused:UNUSED_PAD src0_sel:WORD_1 src1_sel:DWORD
	v_mov_b32_e32 v20, v34
	v_and_b32_sdwa v29, v4, v1 dst_sel:DWORD dst_unused:UNUSED_PAD src0_sel:WORD_1 src1_sel:DWORD
	v_and_b32_sdwa v34, v8, v1 dst_sel:DWORD dst_unused:UNUSED_PAD src0_sel:WORD_1 src1_sel:DWORD
	v_and_b32_sdwa v53, v18, v1 dst_sel:DWORD dst_unused:UNUSED_PAD src0_sel:WORD_1 src1_sel:DWORD
	v_add3_u32 v2, v2, v31, s58
	v_add3_u32 v9, v9, v32, s58
	v_add3_u32 v19, v19, v52, s58
	v_and_b32_sdwa v30, v3, v1 dst_sel:DWORD dst_unused:UNUSED_PAD src0_sel:WORD_1 src1_sel:DWORD
	v_add3_u32 v4, v4, v29, s58
	v_add3_u32 v8, v8, v34, s58
	v_add3_u32 v18, v18, v53, s58
	v_and_b32_e32 v2, 0xffff0000, v2
	v_lshrrev_b32_e32 v9, 16, v9
	v_lshrrev_b32_e32 v19, 16, v19
	v_mov_b32_e32 v32, v35
	v_and_b32_sdwa v28, v5, v1 dst_sel:DWORD dst_unused:UNUSED_PAD src0_sel:WORD_1 src1_sel:DWORD
	v_add3_u32 v3, v3, v30, s58
	v_or_b32_sdwa v2, v2, v4 dst_sel:DWORD dst_unused:UNUSED_PAD src0_sel:DWORD src1_sel:WORD_1
	v_and_or_b32 v4, v8, s57, v9
	v_and_or_b32 v8, v18, s57, v19
	v_pk_mul_f32 v[18:19], v[32:33], v[62:63]
	v_add3_u32 v5, v5, v28, s58
	v_and_b32_e32 v3, 0xffff0000, v3
	v_pk_fma_f32 v[18:19], v[20:21], v[60:61], v[18:19] neg_lo:[0,0,1] neg_hi:[0,0,1]
	v_or_b32_sdwa v3, v3, v5 dst_sel:DWORD dst_unused:UNUSED_PAD src0_sel:DWORD src1_sel:WORD_1
	v_and_b32_sdwa v5, v19, v1 dst_sel:DWORD dst_unused:UNUSED_PAD src0_sel:WORD_1 src1_sel:DWORD
	v_and_b32_sdwa v9, v18, v1 dst_sel:DWORD dst_unused:UNUSED_PAD src0_sel:WORD_1 src1_sel:DWORD
	v_add3_u32 v9, v18, v9, s58
	v_add3_u32 v5, v19, v5, s58
	v_pk_mul_f32 v[18:19], v[32:33], v[60:61]
	v_lshrrev_b32_e32 v5, 16, v5
	v_pk_fma_f32 v[18:19], v[20:21], v[62:63], v[18:19]
	v_and_or_b32 v5, v9, s57, v5
	v_and_b32_sdwa v9, v19, v1 dst_sel:DWORD dst_unused:UNUSED_PAD src0_sel:WORD_1 src1_sel:DWORD
	v_and_b32_sdwa v26, v7, v1 dst_sel:DWORD dst_unused:UNUSED_PAD src0_sel:WORD_1 src1_sel:DWORD
	v_and_b32_sdwa v27, v6, v1 dst_sel:DWORD dst_unused:UNUSED_PAD src0_sel:WORD_1 src1_sel:DWORD
	v_and_b32_sdwa v20, v18, v1 dst_sel:DWORD dst_unused:UNUSED_PAD src0_sel:WORD_1 src1_sel:DWORD
	v_add3_u32 v9, v19, v9, s58
	v_and_b32_sdwa v24, v23, v1 dst_sel:DWORD dst_unused:UNUSED_PAD src0_sel:WORD_1 src1_sel:DWORD
	v_and_b32_sdwa v25, v22, v1 dst_sel:DWORD dst_unused:UNUSED_PAD src0_sel:WORD_1 src1_sel:DWORD
	v_add3_u32 v7, v7, v26, s58
	v_add3_u32 v6, v6, v27, s58
	v_add3_u32 v18, v18, v20, s58
	v_lshrrev_b32_e32 v9, 16, v9
	v_add3_u32 v22, v22, v25, s58
	v_add3_u32 v23, v23, v24, s58
	v_and_b32_e32 v7, 0xffff0000, v7
	v_and_b32_e32 v6, 0xffff0000, v6
	v_and_or_b32 v9, v18, s57, v9
	v_lshlrev_b32_e32 v19, 16, v11
	v_lshlrev_b32_e32 v18, 16, v10
	s_waitcnt vmcnt(1)
	v_mov_b32_e32 v25, v44
	s_waitcnt vmcnt(0)
	v_mov_b32_e32 v44, v49
	v_or_b32_sdwa v7, v7, v23 dst_sel:DWORD dst_unused:UNUSED_PAD src0_sel:DWORD src1_sel:WORD_1
	v_or_b32_sdwa v6, v6, v22 dst_sel:DWORD dst_unused:UNUSED_PAD src0_sel:DWORD src1_sel:WORD_1
	v_lshlrev_b32_e32 v21, 16, v15
	v_lshlrev_b32_e32 v20, 16, v14
	v_and_b32_e32 v23, 0xffff0000, v15
	v_and_b32_e32 v22, 0xffff0000, v14
	v_mov_b32_e32 v24, v48
	v_pk_mul_f32 v[14:15], v[44:45], v[18:19]
	v_mov_b32_e32 v27, v46
	v_pk_fma_f32 v[14:15], v[24:25], v[20:21], v[14:15]
	v_mov_b32_e32 v46, v51
	v_pk_mul_f32 v[20:21], v[44:45], v[20:21]
	v_and_b32_e32 v11, 0xffff0000, v11
	v_and_b32_e32 v10, 0xffff0000, v10
	v_mov_b32_e32 v26, v50
	v_pk_fma_f32 v[18:19], v[24:25], v[18:19], v[20:21] neg_lo:[0,0,1] neg_hi:[0,0,1]
	v_pk_mul_f32 v[20:21], v[46:47], v[22:23]
	v_pk_mul_f32 v[28:29], v[46:47], v[10:11]
	v_pk_fma_f32 v[10:11], v[26:27], v[10:11], v[20:21] neg_lo:[0,0,1] neg_hi:[0,0,1]
	v_and_b32_sdwa v20, v19, v1 dst_sel:DWORD dst_unused:UNUSED_PAD src0_sel:WORD_1 src1_sel:DWORD
	v_and_b32_sdwa v21, v18, v1 dst_sel:DWORD dst_unused:UNUSED_PAD src0_sel:WORD_1 src1_sel:DWORD
	v_add3_u32 v18, v18, v21, s58
	v_add3_u32 v19, v19, v20, s58
	v_and_b32_sdwa v20, v11, v1 dst_sel:DWORD dst_unused:UNUSED_PAD src0_sel:WORD_1 src1_sel:DWORD
	v_and_b32_sdwa v21, v10, v1 dst_sel:DWORD dst_unused:UNUSED_PAD src0_sel:WORD_1 src1_sel:DWORD
	v_add3_u32 v11, v11, v20, s58
	v_add3_u32 v10, v10, v21, s58
	v_pk_fma_f32 v[28:29], v[26:27], v[22:23], v[28:29]
	v_and_b32_e32 v11, 0xffff0000, v11
	v_and_b32_e32 v10, 0xffff0000, v10
	v_and_b32_e32 v20, 0xffff0000, v16
	v_lshlrev_b32_e32 v21, 16, v16
	v_mov_b32_e32 v23, v40
	v_mov_b32_e32 v40, v43
	v_or_b32_sdwa v11, v11, v19 dst_sel:DWORD dst_unused:UNUSED_PAD src0_sel:DWORD src1_sel:WORD_1
	v_or_b32_sdwa v10, v10, v18 dst_sel:DWORD dst_unused:UNUSED_PAD src0_sel:DWORD src1_sel:WORD_1
	v_and_b32_e32 v18, 0xffff0000, v12
	v_lshlrev_b32_e32 v19, 16, v12
	v_mov_b32_e32 v22, v42
	v_pk_mul_f32 v[24:25], v[40:41], v[20:21]
	v_and_b32_sdwa v30, v15, v1 dst_sel:DWORD dst_unused:UNUSED_PAD src0_sel:WORD_1 src1_sel:DWORD
	v_pk_fma_f32 v[24:25], v[22:23], v[18:19], v[24:25] neg_lo:[0,0,1] neg_hi:[0,0,1]
	v_pk_mul_f32 v[18:19], v[40:41], v[18:19]
	v_and_b32_sdwa v12, v25, v1 dst_sel:DWORD dst_unused:UNUSED_PAD src0_sel:WORD_1 src1_sel:DWORD
	v_and_b32_sdwa v16, v24, v1 dst_sel:DWORD dst_unused:UNUSED_PAD src0_sel:WORD_1 src1_sel:DWORD
	v_add3_u32 v12, v25, v12, s58
	v_add3_u32 v16, v24, v16, s58
	v_lshrrev_b32_e32 v12, 16, v12
	v_pk_fma_f32 v[18:19], v[22:23], v[20:21], v[18:19]
	v_and_or_b32 v12, v16, s57, v12
	v_and_b32_sdwa v16, v19, v1 dst_sel:DWORD dst_unused:UNUSED_PAD src0_sel:WORD_1 src1_sel:DWORD
	v_and_b32_sdwa v20, v18, v1 dst_sel:DWORD dst_unused:UNUSED_PAD src0_sel:WORD_1 src1_sel:DWORD
	v_add3_u32 v16, v19, v16, s58
	v_add3_u32 v18, v18, v20, s58
	v_lshrrev_b32_e32 v16, 16, v16
	v_and_b32_e32 v20, 0xffff0000, v17
	v_lshlrev_b32_e32 v21, 16, v17
	v_mov_b32_e32 v23, v36
	v_mov_b32_e32 v36, v39
	v_and_or_b32 v16, v18, s57, v16
	v_and_b32_e32 v18, 0xffff0000, v13
	v_lshlrev_b32_e32 v19, 16, v13
	v_mov_b32_e32 v22, v38
	v_pk_mul_f32 v[24:25], v[36:37], v[20:21]
	v_and_b32_sdwa v31, v14, v1 dst_sel:DWORD dst_unused:UNUSED_PAD src0_sel:WORD_1 src1_sel:DWORD
	v_pk_fma_f32 v[24:25], v[22:23], v[18:19], v[24:25] neg_lo:[0,0,1] neg_hi:[0,0,1]
	v_pk_mul_f32 v[18:19], v[36:37], v[18:19]
	v_and_b32_sdwa v13, v25, v1 dst_sel:DWORD dst_unused:UNUSED_PAD src0_sel:WORD_1 src1_sel:DWORD
	v_and_b32_sdwa v17, v24, v1 dst_sel:DWORD dst_unused:UNUSED_PAD src0_sel:WORD_1 src1_sel:DWORD
	v_add3_u32 v13, v25, v13, s58
	v_add3_u32 v17, v24, v17, s58
	v_lshrrev_b32_e32 v13, 16, v13
	v_pk_fma_f32 v[18:19], v[22:23], v[20:21], v[18:19]
	v_add3_u32 v14, v14, v31, s58
	v_add3_u32 v15, v15, v30, s58
	v_and_b32_sdwa v30, v29, v1 dst_sel:DWORD dst_unused:UNUSED_PAD src0_sel:WORD_1 src1_sel:DWORD
	v_and_b32_sdwa v31, v28, v1 dst_sel:DWORD dst_unused:UNUSED_PAD src0_sel:WORD_1 src1_sel:DWORD
	v_and_or_b32 v13, v17, s57, v13
	v_and_b32_sdwa v17, v19, v1 dst_sel:DWORD dst_unused:UNUSED_PAD src0_sel:WORD_1 src1_sel:DWORD
	v_add3_u32 v29, v29, v30, s58
	v_add3_u32 v28, v28, v31, s58
	v_and_b32_sdwa v20, v18, v1 dst_sel:DWORD dst_unused:UNUSED_PAD src0_sel:WORD_1 src1_sel:DWORD
	v_add3_u32 v17, v19, v17, s58
	v_and_b32_e32 v29, 0xffff0000, v29
	v_and_b32_e32 v28, 0xffff0000, v28
	v_add3_u32 v18, v18, v20, s58
	v_lshrrev_b32_e32 v17, 16, v17
	v_or_b32_sdwa v15, v29, v15 dst_sel:DWORD dst_unused:UNUSED_PAD src0_sel:DWORD src1_sel:WORD_1
	v_or_b32_sdwa v14, v28, v14 dst_sel:DWORD dst_unused:UNUSED_PAD src0_sel:DWORD src1_sel:WORD_1
	v_and_or_b32 v17, v18, s57, v17
